# attention unit start: wait before the first QK MFMA leaves the just-issued K/V DMA of tile 2 in flight (vmcnt(4) instead of vmcnt(0))
# baseline (speedup 1.0000x reference)
; __device__ __forceinline__ int a2_crow(int r, int hi) { return (r & 3) + 8 * (r >> 2) + 4 * hi; }
; __device__ __forceinline__ int a2_crow(int r, int hi) { return (r & 3) + 8 * (r >> 2) + 4 * hi; }
; #define A3_PSM(p_, al_, n, h) a3_psm(p_, m_reg, al_, A3_MASKED(n, h), A3_KB(n, h) - qt, hi)
; #define A3_BAR() do { asm volatile("s_waitcnt lgkmcnt(0)" ::: "memory"); __builtin_amdgcn_s_barrier(); asm volatile("" ::: "memory"); } while (0)
; #define A3_PSM(p_, al_, n, h) a3_psm(p_, m_reg, al_, A3_MASKED(n, h), A3_KB(n, h) - qt, hi)
; #define A3_BAR() do { asm volatile("s_waitcnt lgkmcnt(0)" ::: "memory"); __builtin_amdgcn_s_barrier(); asm volatile("" ::: "memory"); } while (0)
; __device__ __forceinline__ void a3_psm(f32x16& p, float& m_reg, float& alpha, bool need_mask, int kd, int hi) {
;     if (need_mask) {
; #pragma unroll
;         for (int r = 0; r < 16; ++r) { const int d = kd + a2_crow(r, hi); if (d > WIN || d < -WIN) p[r] = -INFINITY; }
;     }
; __device__ __forceinline__ void attn_stream(Frame& F, const float* sinkl, int u_first, int u_stride, int n_lat, int u_extra) {
;     ...
;         if (ui == 0) asm volatile("s_waitcnt vmcnt(4)" ::: "memory");
;         A3_BAR();
;         A3S_DMA(cu, 2, rb + 2);
;         { const int b0 = (rb & 3) * A3_BUF;
;           a3_qk(pE, lds + b0 + A3_K, qr, kbase); A3_PSM(pE, alE, 0, 0);
.LBB13_523:
	s_add_i32 s23, s36, s35
	s_lshl_b32 s4, s53, 8
	s_add_u32 s4, s8, s4
	s_addc_u32 s5, s9, 0
	s_lshl_b32 s6, s61, 6
	s_sub_i32 s6, s20, s6
	s_cmp_gt_i32 s61, 2
	s_cselect_b32 s6, s68, s6
	s_addk_i32 s6, 0x80
	s_mul_hi_i32 s7, s6, 0x2c00
	s_mulk_i32 s6, 0x2c00
	s_add_u32 s4, s4, s6
	s_addc_u32 s5, s5, s7
	s_lshl_b32 s37, s58, 15
	s_and_b32 s26, s37, 0x18000
	s_xor_b32 s6, s26, 0x10000
	v_lshl_add_u64 v[2:3], s[4:5], 0, v[132:133]
	s_add_i32 s6, s52, s6
	s_waitcnt lgkmcnt(0)
	s_barrier
	v_lshl_add_u64 v[2:3], v[2:3], 0, s[96:97]
	s_mov_b32 m0, s6
	v_add_u32_e32 v144, s23, v99
	global_load_lds_dwordx4 v[2:3], off
	v_lshl_add_u64 v[2:3], s[4:5], 0, v[134:135]
	v_lshl_add_u64 v[2:3], v[2:3], 0, s[84:85]
	s_add_i32 m0, s6, 0x4000
	s_nop 0
	global_load_lds_dwordx4 v[2:3], off
	v_lshl_add_u64 v[2:3], s[4:5], 0, v[136:137]
	v_lshl_add_u64 v[2:3], v[2:3], 0, s[96:97]
	s_add_i32 m0, s6, 0x400
	s_nop 0
	global_load_lds_dwordx4 v[2:3], off
	v_lshl_add_u64 v[2:3], s[4:5], 0, v[138:139]
	v_lshl_add_u64 v[2:3], v[2:3], 0, s[84:85]
	s_add_i32 m0, s6, 0x4400
	s_add_i32 s4, s57, s26
	global_load_lds_dwordx4 v[2:3], off
	v_add_u32_e32 v25, s4, v151
	ds_read_b128 v[2:5], v25 offset:16384
	s_setprio 1
	s_waitcnt vmcnt(4) lgkmcnt(0)
	v_mfma_f32_32x32x16_bf16 v[2:17], v[2:5], v[100:103], 0
	s_setprio 0
	v_add_u32_e32 v18, s4, v153
	ds_read_b128 v[20:23], v18 offset:16384
	s_setprio 1
	s_waitcnt lgkmcnt(0)
	v_mfma_f32_32x32x16_bf16 v[2:17], v[20:23], v[104:107], v[2:17]
	s_setprio 0
	v_add_u32_e32 v19, s4, v154
	ds_read_b128 v[20:23], v19 offset:16384
	s_setprio 1
	s_waitcnt lgkmcnt(0)
	v_mfma_f32_32x32x16_bf16 v[2:17], v[20:23], v[108:111], v[2:17]
	s_setprio 0
	v_add_u32_e32 v20, s4, v155
	ds_read_b128 v[28:31], v20 offset:16384
	s_setprio 1
	s_waitcnt lgkmcnt(0)
	v_mfma_f32_32x32x16_bf16 v[2:17], v[28:31], v[112:115], v[2:17]
	s_setprio 0
	v_add_u32_e32 v21, s4, v156
	ds_read_b128 v[28:31], v21 offset:16384
	s_setprio 1
	s_waitcnt lgkmcnt(0)
	v_mfma_f32_32x32x16_bf16 v[2:17], v[28:31], v[116:119], v[2:17]
	s_setprio 0
	v_add_u32_e32 v22, s4, v157
	ds_read_b128 v[28:31], v22 offset:16384
	s_setprio 1
	s_waitcnt lgkmcnt(0)
	v_mfma_f32_32x32x16_bf16 v[2:17], v[28:31], v[120:123], v[2:17]
	s_setprio 0
	v_add_u32_e32 v23, s4, v158
	ds_read_b128 v[28:31], v23 offset:16384
	s_setprio 1
	s_waitcnt lgkmcnt(0)
	v_mfma_f32_32x32x16_bf16 v[2:17], v[28:31], v[124:127], v[2:17]
	s_setprio 0
	v_add_u32_e32 v24, s4, v159
	ds_read_b128 v[28:31], v24 offset:16384
	s_setprio 1
	s_waitcnt lgkmcnt(0)
	v_mfma_f32_32x32x16_bf16 v[2:17], v[28:31], v[128:131], v[2:17]
	s_setprio 0
	s_cmp_gt_i32 s61, 0
	s_cselect_b64 s[6:7], -1, 0
	s_cmp_lt_i32 s61, 1
	s_cbranch_scc1 .LBB13_528
	s_sub_i32 s4, s64, s23
	s_sub_i32 s5, s23, s64
	s_max_i32 s4, s4, s5
	s_cmpk_lt_i32 s4, 0x62
	s_cbranch_scc1 .LBB13_528
	v_sub_u32_e32 v27, v160, v144
	v_add_u32_e32 v27, s64, v27
	v_cmp_lt_u32_e32 vcc, s65, v27
	v_add_u32_e32 v28, 1, v27
	s_nop 0
	v_cndmask_b32_e32 v2, v239, v2, vcc
	v_cmp_lt_u32_e32 vcc, s65, v28
	v_add_u32_e32 v28, 2, v27
	s_nop 0
	v_cndmask_b32_e32 v3, v239, v3, vcc
	v_cmp_lt_u32_e32 vcc, s65, v28
	v_add_u32_e32 v28, 3, v27
	s_nop 0
	v_cndmask_b32_e32 v4, v239, v4, vcc
	v_cmp_lt_u32_e32 vcc, s65, v28
	v_add_u32_e32 v28, 8, v27
	s_nop 0
	v_cndmask_b32_e32 v5, v239, v5, vcc
	v_cmp_lt_u32_e32 vcc, s65, v28
	v_add_u32_e32 v28, 9, v27
	s_nop 0
	v_cndmask_b32_e32 v6, v239, v6, vcc
	v_cmp_lt_u32_e32 vcc, s65, v28
	v_add_u32_e32 v28, 10, v27
	s_nop 0
	v_cndmask_b32_e32 v7, v239, v7, vcc
	v_cmp_lt_u32_e32 vcc, s65, v28
	v_add_u32_e32 v28, 11, v27
	s_nop 0
	v_cndmask_b32_e32 v8, v239, v8, vcc
	v_cmp_lt_u32_e32 vcc, s65, v28
	v_add_u32_e32 v28, 16, v27
	s_nop 0
	v_cndmask_b32_e32 v9, v239, v9, vcc
	v_cmp_lt_u32_e32 vcc, s65, v28
	v_add_u32_e32 v28, 17, v27
	s_nop 0
	v_cndmask_b32_e32 v10, v239, v10, vcc
	v_cmp_lt_u32_e32 vcc, s65, v28
	v_add_u32_e32 v28, 18, v27
	s_nop 0
	v_cndmask_b32_e32 v11, v239, v11, vcc
	v_cmp_lt_u32_e32 vcc, s65, v28
	v_add_u32_e32 v28, 19, v27
	s_nop 0
	v_cndmask_b32_e32 v12, v239, v12, vcc
	v_cmp_lt_u32_e32 vcc, s65, v28
	v_add_u32_e32 v28, 24, v27
	s_nop 0
	v_cndmask_b32_e32 v13, v239, v13, vcc
	v_cmp_lt_u32_e32 vcc, s65, v28
	v_add_u32_e32 v28, 25, v27
	s_nop 0
	v_cndmask_b32_e32 v14, v239, v14, vcc
	v_cmp_lt_u32_e32 vcc, s65, v28
	v_add_u32_e32 v28, 26, v27
	v_add_u32_e32 v27, 27, v27
	v_cndmask_b32_e32 v15, v239, v15, vcc
	v_cmp_lt_u32_e32 vcc, s65, v28
	s_nop 1
	v_cndmask_b32_e32 v16, v239, v16, vcc
	v_cmp_gt_u32_e32 vcc, s67, v27
	s_and_saveexec_b64 s[4:5], vcc
	v_mov_b32_e32 v17, s66
	s_or_b64 exec, exec, s[4:5]
